# P7/P8 accumulator start values copied with 64-bit moves (on top of the P8 bias-as-start-value version)
# speedup vs baseline: 1.0016x; 1.0016x over previous
.LBB0_783:
	v_and_b32_e32 v1, 48, v178
	v_lshlrev_b32_e32 v4, 2, v200
	v_lshl_or_b32 v2, s11, 6, v200
	v_lshl_or_b32 v3, v200, 6, v1
	s_lshl_b32 s11, s11, 13
	v_and_b32_e32 v4, 32, v4
	s_lshl_b32 s5, s5, 5
	v_bitop3_b32 v202, v3, s11, v4 bitop3:0xde
	s_and_b32 s5, s5, 0x60
	v_lshlrev_b32_e32 v3, 6, v178
	s_movk_i32 s11, 0x3c0
	v_and_or_b32 v1, v3, s11, v1
	s_lshl_b32 s11, s5, 7
	s_add_u32 s18, s6, 0x4000
	s_addc_u32 s19, s7, 0
	s_add_i32 s53, s46, 0x8000
	v_lshl_add_u64 v[4:5], s[18:19], 0, v[176:177]
	s_mov_b32 m0, s53
	s_add_i32 s54, s46, 0xa000
	s_waitcnt vmcnt(4)
	s_barrier
	global_load_lds_dwordx4 v[4:5], off
	v_lshl_add_u64 v[4:5], s[18:19], 0, v[180:181]
	s_add_u32 s18, s90, 0xd040080
	s_mov_b32 m0, s54
	s_addc_u32 s19, s91, 0
	global_load_lds_dwordx4 v[4:5], off
	s_add_i32 m0, s46, 0x18000
	v_lshl_add_u64 v[4:5], s[18:19], 0, v[182:183]
	global_load_lds_dwordx4 v[4:5], off
	s_add_i32 m0, s46, 0x1a000
	v_lshl_add_u64 v[4:5], s[18:19], 0, v[184:185]
	s_add_u32 s18, s6, 0x404000
	s_addc_u32 s19, s7, 0
	s_add_i32 s55, s46, 0xc000
	global_load_lds_dwordx4 v[4:5], off
	v_lshl_add_u64 v[4:5], s[18:19], 0, v[176:177]
	s_mov_b32 m0, s55
	s_add_i32 s56, s46, 0xe000
	global_load_lds_dwordx4 v[4:5], off
	v_lshl_add_u64 v[4:5], s[18:19], 0, v[180:181]
	s_mov_b32 m0, s56
	v_lshlrev_b32_e32 v3, 2, v178
	global_load_lds_dwordx4 v[4:5], off
	v_and_b32_e32 v3, 32, v3
	v_bitop3_b32 v6, s11, v1, v3 bitop3:0xf6
	v_mov_b32_e32 v1, v183
	v_lshl_add_u64 v[186:187], s[16:17], 0, v[0:1]
	s_ashr_i32 s17, s33, 31
	s_lshr_b32 s17, s17, 29
	s_add_i32 s17, s33, s17
	s_and_b32 s18, s17, -8
	s_ashr_i32 s16, s96, 3
	s_sub_i32 s18, s33, s18
	s_mul_i32 s16, s16, s18
	s_ashr_i32 s17, s17, 3
	s_add_i32 s18, s16, s17
	s_add_u32 s16, s90, s5
	s_addc_u32 s17, s91, 0
	s_and_b64 s[2:3], s[2:3], exec
	s_mov_b32 s2, 0x20944
	s_cselect_b32 s57, s18, s33
	s_add_i32 s58, s2, 0x100
	s_mov_b32 s2, 0x20948
	s_add_i32 s59, s2, 0x100
	s_mov_b32 s2, 0x2094c
	s_add_i32 s60, s2, 0x100
	s_mov_b32 s2, 0x20950
	s_add_i32 s61, s2, 0x100
	s_mov_b32 s2, 0x20954
	s_add_i32 s62, s2, 0x100
	s_mov_b32 s2, 0x20958
	s_add_i32 s63, s2, 0x100
	s_mov_b32 s2, 0x2095c
	s_add_i32 s64, s2, 0x100
	s_mov_b32 s2, 0x20960
	s_add_i32 s65, s2, 0x100
	s_mov_b32 s2, 0x20964
	s_add_i32 s68, s2, 0x100
	s_mov_b32 s2, 0x20968
	s_add_i32 s69, s2, 0x100
	s_mov_b32 s2, 0x2096c
	s_add_i32 s70, s2, 0x100
	s_mov_b32 s2, 0x20970
	s_addk_i32 s2, 0x100
	v_writelane_b32 v250, s2, 4
	s_mov_b32 s2, 0x20974
	s_addk_i32 s2, 0x100
	v_writelane_b32 v250, s2, 3
	s_mov_b32 s2, 0x20978
	s_addk_i32 s2, 0x100
	v_writelane_b32 v250, s2, 5
	s_mov_b32 s2, 0x2097c
	s_addk_i32 s2, 0x100
	v_writelane_b32 v250, s2, 6
	s_mov_b32 s2, 0x20980
	s_addk_i32 s2, 0x100
	v_writelane_b32 v250, s2, 7
	s_mov_b32 s2, 0x20984
	s_addk_i32 s2, 0x100
	v_writelane_b32 v250, s2, 8
	s_mov_b32 s2, 0x20988
	s_addk_i32 s2, 0x100
	v_writelane_b32 v250, s2, 9
	s_mov_b32 s2, 0x2098c
	s_addk_i32 s2, 0x100
	v_writelane_b32 v250, s2, 10
	s_mov_b32 s2, 0x20990
	s_addk_i32 s2, 0x100
	v_writelane_b32 v250, s2, 11
	s_mov_b32 s2, 0x20994
	s_addk_i32 s2, 0x100
	v_writelane_b32 v250, s2, 12
	s_mov_b32 s2, 0x20998
	s_addk_i32 s2, 0x100
	v_writelane_b32 v250, s2, 13
	s_mov_b32 s2, 0x2099c
	s_addk_i32 s2, 0x100
	v_writelane_b32 v250, s2, 14
	s_mov_b32 s2, 0x209a0
	s_addk_i32 s2, 0x100
	v_writelane_b32 v250, s2, 15
	s_mov_b32 s2, 0x209a4
	s_addk_i32 s2, 0x100
	v_writelane_b32 v250, s2, 16
	s_mov_b32 s2, 0x209a8
	s_addk_i32 s2, 0x100
	v_writelane_b32 v250, s2, 17
	s_mov_b32 s2, 0x209ac
	s_addk_i32 s2, 0x100
	v_writelane_b32 v250, s2, 18
	s_mov_b32 s2, 0x209b0
	s_addk_i32 s2, 0x100
	v_writelane_b32 v250, s2, 19
	s_mov_b32 s2, 0x209b4
	s_addk_i32 s2, 0x100
	v_writelane_b32 v250, s2, 20
	s_mov_b32 s2, 0x209b8
	s_addk_i32 s2, 0x100
	v_and_b32_e32 v4, 12, v218
	v_mov_b32_e32 v5, v183
	v_mov_b32_e32 v3, v183
	v_writelane_b32 v250, s2, 21
	s_mov_b32 s2, 0x209bc
	s_waitcnt vmcnt(6)
	v_lshlrev_b64 v[2:3], 7, v[2:3]
	v_lshl_add_u64 v[0:1], s[16:17], 0, v[4:5]
	s_addk_i32 s2, 0x100
	s_mov_b32 s11, 0x18000
	v_lshl_add_u64 v[0:1], v[0:1], 0, v[2:3]
	s_mov_b64 s[16:17], 0xf1a0000
	v_writelane_b32 v250, s2, 22
	s_mov_b32 s2, 0x14000
	v_lshl_add_u64 v[188:189], v[0:1], 0, s[16:17]
	v_mov_b32_e32 v203, 0x7f7f7f7f
	v_mov_b32_e32 v204, 0x79797979
	s_add_i32 s79, s2, 0x100
	s_mov_b64 s[16:17], 0x80
	s_lshl_b32 s73, s5, 2
	v_lshlrev_b32_e32 v194, 2, v4
	s_mov_b32 s80, 0xc0c00000
	s_mov_b32 s81, 0xc3e00000
	v_add_u32_e32 v205, 0x100, v6
	s_add_i32 s77, s11, 0x100
	v_mov_b32_e32 v206, 0x41000000
	v_mov_b32_e32 v207, 0x43e00000
	s_lshl_b32 s99, s4, 14
	s_lshl_b32 s100, s10, 2
	s_add_u32 s99, s99, s100
	s_add_u32 s99, s99, s73
	s_add_u32 s100, s82, s99
	s_addc_u32 s101, s83, 0
	global_load_dwordx4 v[172:175], v194, s[100:101]
	global_load_dwordx4 v[168:171], v194, s[100:101] offset:64
	s_add_u32 s100, s100, 0x2000
	s_addc_u32 s101, s101, 0
	global_load_dwordx4 v[140:143], v194, s[100:101]
	global_load_dwordx4 v[136:139], v194, s[100:101] offset:64
	s_waitcnt vmcnt(0)
	v_add_f32_e32 v140, 1.0, v140
	v_add_f32_e32 v141, 1.0, v141
	v_add_f32_e32 v142, 1.0, v142
	v_add_f32_e32 v143, 1.0, v143
	v_add_f32_e32 v136, 1.0, v136
	v_add_f32_e32 v137, 1.0, v137
	v_add_f32_e32 v138, 1.0, v138
	v_add_f32_e32 v139, 1.0, v139
	v_mov_b64_e32 v[164:165], v[172:173]
	v_mov_b64_e32 v[166:167], v[174:175]
	v_mov_b64_e32 v[160:161], v[168:169]
	v_mov_b64_e32 v[162:163], v[170:171]
	v_mov_b64_e32 v[156:157], v[172:173]
	v_mov_b64_e32 v[158:159], v[174:175]
	v_mov_b64_e32 v[152:153], v[168:169]
	v_mov_b64_e32 v[154:155], v[170:171]
	v_mov_b64_e32 v[148:149], v[172:173]
	v_mov_b64_e32 v[150:151], v[174:175]
	v_mov_b64_e32 v[144:145], v[168:169]
	v_mov_b64_e32 v[146:147], v[170:171]
	v_mov_b64_e32 v[132:133], v[140:141]
	v_mov_b64_e32 v[134:135], v[142:143]
	v_mov_b64_e32 v[128:129], v[136:137]
	v_mov_b64_e32 v[130:131], v[138:139]
	v_mov_b64_e32 v[124:125], v[140:141]
	v_mov_b64_e32 v[126:127], v[142:143]
	v_mov_b64_e32 v[120:121], v[136:137]
	v_mov_b64_e32 v[122:123], v[138:139]
	v_mov_b64_e32 v[116:117], v[140:141]
	v_mov_b64_e32 v[118:119], v[142:143]
	v_mov_b64_e32 v[112:113], v[136:137]
	v_mov_b64_e32 v[114:115], v[138:139]
	v_mov_b64_e32 v[108:109], v[172:173]
	v_mov_b64_e32 v[110:111], v[174:175]
	v_mov_b64_e32 v[104:105], v[168:169]
	v_mov_b64_e32 v[106:107], v[170:171]
	v_mov_b64_e32 v[100:101], v[172:173]
	v_mov_b64_e32 v[102:103], v[174:175]
	v_mov_b64_e32 v[96:97], v[168:169]
	v_mov_b64_e32 v[98:99], v[170:171]
	v_mov_b64_e32 v[92:93], v[172:173]
	v_mov_b64_e32 v[94:95], v[174:175]
	v_mov_b64_e32 v[88:89], v[168:169]
	v_mov_b64_e32 v[90:91], v[170:171]
	v_mov_b64_e32 v[84:85], v[172:173]
	v_mov_b64_e32 v[86:87], v[174:175]
	v_mov_b64_e32 v[80:81], v[168:169]
	v_mov_b64_e32 v[82:83], v[170:171]
	v_mov_b64_e32 v[76:77], v[140:141]
	v_mov_b64_e32 v[78:79], v[142:143]
	v_mov_b64_e32 v[72:73], v[136:137]
	v_mov_b64_e32 v[74:75], v[138:139]
	v_mov_b64_e32 v[68:69], v[140:141]
	v_mov_b64_e32 v[70:71], v[142:143]
	v_mov_b64_e32 v[64:65], v[136:137]
	v_mov_b64_e32 v[66:67], v[138:139]
	v_mov_b64_e32 v[60:61], v[140:141]
	v_mov_b64_e32 v[62:63], v[142:143]
	v_mov_b64_e32 v[56:57], v[136:137]
	v_mov_b64_e32 v[58:59], v[138:139]
	v_mov_b64_e32 v[52:53], v[140:141]
	v_mov_b64_e32 v[54:55], v[142:143]
	v_mov_b64_e32 v[48:49], v[136:137]
	v_mov_b64_e32 v[50:51], v[138:139]
	s_barrier
	s_branch .LBB0_785

.LBB0_827:
	s_ashr_i32 s5, s4, 31
	s_lshl_b64 s[26:27], s[4:5], 14
	s_add_u32 s5, s82, s26
	s_addc_u32 s23, s83, s27
	s_ashr_i32 s11, s10, 31
	s_lshl_b64 s[26:27], s[10:11], 2
	s_add_u32 s5, s5, s26
	s_addc_u32 s11, s23, s27
	s_add_u32 s26, s5, s73
	s_addc_u32 s27, s11, 0
	v_mov_b32_e32 v195, v183
	s_movk_i32 s5, 0x2000
	v_mov_b32_e32 v18, v183
	s_nop 0
	s_nop 0
	s_ashr_i32 s5, s45, 3
	s_ashr_i32 s11, s10, 7
	s_and_b32 s5, s5, -16
	s_add_i32 s26, s5, s11
	s_ashr_i32 s27, s26, 31
	s_lshl_b64 s[26:27], s[26:27], 14
	v_lshl_add_u64 v[16:17], v[188:189], 0, s[26:27]
	s_movk_i32 s5, 0x1000
	s_mov_b64 s[26:27], 0x40000
	v_bfe_u32 v251, v178, 4, 2
	v_mov_b32_e32 v255, 0
	v_mul_u32_u24_e32 v254, 0x7fc, v251
	v_lshl_add_u64 v[252:253], v[16:17], 0, v[254:255]
	v_lshl_add_u64 v[254:255], v[252:253], 0, s[26:27]
	v_min_f32_e32 v19, 0x40e00000, v172
	v_min_f32_e32 v20, 0x40e00000, v173
	v_mul_f32_e32 v27, 0xc01d265f, v19
	v_mul_f32_e32 v29, 0xc01d265f, v20
	v_exp_f32_e32 v27, v27
	v_exp_f32_e32 v29, v29
	v_min_f32_e32 v21, 0x40e00000, v174
	v_min_f32_e32 v22, 0x40e00000, v175
	v_mul_f32_e32 v31, 0xc01d265f, v21
	v_mul_f32_e32 v33, 0xc01d265f, v22
	v_min_f32_e32 v23, 0x40e00000, v168
	v_exp_f32_e32 v31, v31
	v_exp_f32_e32 v33, v33
	v_add_f32_e32 v27, 1.0, v27
	v_add_f32_e32 v29, 1.0, v29
	v_mul_f32_e32 v35, 0xc01d265f, v23
	v_rcp_f32_e32 v27, v27
	v_rcp_f32_e32 v29, v29
	v_exp_f32_e32 v35, v35
	v_med3_f32 v26, v140, s80, v206
	v_med3_f32 v28, v141, s80, v206
	v_add_f32_e32 v31, 1.0, v31
	v_add_f32_e32 v33, 1.0, v33
	v_rcp_f32_e32 v31, v31
	v_rcp_f32_e32 v33, v33
	v_mul_f32_e32 v19, v19, v27
	v_mul_f32_e32 v20, v20, v29
	v_min_f32_e32 v25, 0x40e00000, v170
	v_mul_f32_e32 v19, v26, v19
	v_mul_f32_e32 v20, v28, v20
	v_mul_f32_e32 v38, 0xc01d265f, v25
	v_add_f32_e32 v35, 1.0, v35
	v_med3_f32 v30, v142, s80, v206
	v_med3_f32 v32, v143, s80, v206
	v_rcp_f32_e32 v35, v35
	v_cvt_pk_fp8_f32 v18, v19, v20
	v_exp_f32_e32 v38, v38
	v_mul_f32_e32 v21, v21, v31
	v_mul_f32_e32 v22, v22, v33
	v_min_f32_e32 v24, 0x40e00000, v169
	v_mul_f32_e32 v21, v30, v21
	v_mul_f32_e32 v22, v32, v22
	v_mul_f32_e32 v37, 0xc01d265f, v24
	v_med3_f32 v34, v136, s80, v206
	v_mov_b32_e32 v20, v21
	v_mov_b32_e32 v21, v22
	v_mul_f32_e32 v23, v23, v35
	v_cvt_pk_fp8_f32 v18, v20, v21 op_sel:[0,0,1]
	v_min_f32_e32 v22, 0x40e00000, v171
	v_exp_f32_e32 v37, v37
	v_mul_f32_e32 v19, v34, v23
	v_add_f32_e32 v21, 1.0, v38
	v_mul_f32_e32 v23, 0xc01d265f, v22
	v_rcp_f32_e32 v21, v21
	v_exp_f32_e32 v23, v23
	v_mov_b32_e32 v236, v18
	v_add_f32_e32 v37, 1.0, v37
	v_med3_f32 v18, v138, s80, v206
	v_rcp_f32_e32 v37, v37
	v_mul_f32_e32 v21, v25, v21
	v_mul_f32_e32 v18, v18, v21
	v_add_f32_e32 v21, 1.0, v23
	v_rcp_f32_e32 v21, v21
	v_med3_f32 v36, v137, s80, v206
	v_mul_f32_e32 v24, v24, v37
	v_mul_f32_e32 v20, v36, v24
	v_mul_f32_e32 v21, v22, v21
	v_mov_b32_e32 v22, v183
	v_cvt_pk_fp8_f32 v22, v19, v20
	v_med3_f32 v19, v139, s80, v206
	s_lshl_b32 s99, s18, 14
	s_lshl_b32 s100, s19, 2
	s_add_u32 s99, s99, s100
	s_add_u32 s99, s99, s73
	s_add_u32 s100, s82, s99
	s_addc_u32 s101, s83, 0
	global_load_dwordx4 v[172:175], v194, s[100:101]
	global_load_dwordx4 v[168:171], v194, s[100:101] offset:64
	s_add_u32 s100, s100, 0x2000
	s_addc_u32 s101, s101, 0
	global_load_dwordx4 v[140:143], v194, s[100:101]
	global_load_dwordx4 v[136:139], v194, s[100:101] offset:64
	v_mul_f32_e32 v19, v19, v21
	v_cvt_pk_fp8_f32 v22, v18, v19 op_sel:[0,0,1]
	v_min_f32_e32 v18, 0x40e00000, v164
	v_mul_f32_e32 v19, 0xc01d265f, v18
	v_exp_f32_e32 v19, v19
	v_min_f32_e32 v21, 0x40e00000, v165
	v_mov_b32_e32 v240, v22
	v_add_f32_e32 v19, 1.0, v19
	v_mul_f32_e32 v22, 0xc01d265f, v21
	v_rcp_f32_e32 v19, v19
	v_exp_f32_e32 v22, v22
	v_mul_f32_e32 v18, v18, v19
	v_med3_f32 v19, v132, s80, v206
	v_mul_f32_e32 v18, v19, v18
	v_add_f32_e32 v19, 1.0, v22
	v_rcp_f32_e32 v19, v19
	v_med3_f32 v20, v133, s80, v206
	v_mul_f32_e32 v19, v21, v19
	v_mul_f32_e32 v19, v20, v19
	v_min_f32_e32 v20, 0x40e00000, v166
	v_mul_f32_e32 v21, 0xc01d265f, v20
	v_exp_f32_e32 v21, v21
	v_min_f32_e32 v23, 0x40e00000, v167
	v_mul_f32_e32 v24, 0xc01d265f, v23
	v_add_f32_e32 v21, 1.0, v21
	v_rcp_f32_e32 v21, v21
	v_exp_f32_e32 v24, v24
	v_mul_f32_e32 v20, v20, v21
	v_med3_f32 v21, v134, s80, v206
	v_mul_f32_e32 v20, v21, v20
	v_add_f32_e32 v21, 1.0, v24
	v_rcp_f32_e32 v21, v21
	s_nop 0
	v_mul_f32_e32 v21, v23, v21
	v_mov_b32_e32 v23, v183
	v_cvt_pk_fp8_f32 v23, v18, v19
	v_med3_f32 v18, v135, s80, v206
	v_mul_f32_e32 v18, v18, v21
	v_cvt_pk_fp8_f32 v23, v20, v18 op_sel:[0,0,1]
	v_min_f32_e32 v18, 0x40e00000, v160
	v_mul_f32_e32 v19, 0xc01d265f, v18
	v_exp_f32_e32 v19, v19
	v_min_f32_e32 v21, 0x40e00000, v161
	v_mul_f32_e32 v22, 0xc01d265f, v21
	v_add_f32_e32 v19, 1.0, v19
	v_rcp_f32_e32 v19, v19
	v_exp_f32_e32 v22, v22
	v_mul_f32_e32 v18, v18, v19
	v_med3_f32 v19, v128, s80, v206
	v_mul_f32_e32 v18, v19, v18
	v_add_f32_e32 v19, 1.0, v22
	v_rcp_f32_e32 v19, v19
	v_med3_f32 v20, v129, s80, v206
	v_mul_f32_e32 v19, v21, v19
	v_mul_f32_e32 v19, v20, v19
	v_min_f32_e32 v20, 0x40e00000, v162
	v_mul_f32_e32 v21, 0xc01d265f, v20
	v_exp_f32_e32 v21, v21
	v_mov_b32_e32 v237, v23
	v_min_f32_e32 v23, 0x40e00000, v163
	v_add_f32_e32 v21, 1.0, v21
	v_mul_f32_e32 v24, 0xc01d265f, v23
	v_rcp_f32_e32 v21, v21
	v_exp_f32_e32 v24, v24
	v_mul_f32_e32 v20, v20, v21
	v_med3_f32 v21, v130, s80, v206
	v_mul_f32_e32 v20, v21, v20
	v_add_f32_e32 v21, 1.0, v24
	v_rcp_f32_e32 v21, v21
	s_nop 0
	v_mul_f32_e32 v21, v23, v21
	v_mov_b32_e32 v23, v183
	v_cvt_pk_fp8_f32 v23, v18, v19
	v_med3_f32 v18, v131, s80, v206
	v_mul_f32_e32 v18, v18, v21
	v_cvt_pk_fp8_f32 v23, v20, v18 op_sel:[0,0,1]
	v_min_f32_e32 v18, 0x40e00000, v156
	v_mul_f32_e32 v19, 0xc01d265f, v18
	v_exp_f32_e32 v19, v19
	v_min_f32_e32 v21, 0x40e00000, v157
	v_mul_f32_e32 v22, 0xc01d265f, v21
	v_add_f32_e32 v19, 1.0, v19
	v_rcp_f32_e32 v19, v19
	v_exp_f32_e32 v22, v22
	v_mul_f32_e32 v18, v18, v19
	v_med3_f32 v19, v124, s80, v206
	v_mul_f32_e32 v18, v19, v18
	v_add_f32_e32 v19, 1.0, v22
	v_rcp_f32_e32 v19, v19
	v_med3_f32 v20, v125, s80, v206
	v_mul_f32_e32 v19, v21, v19
	v_mul_f32_e32 v19, v20, v19
	v_min_f32_e32 v20, 0x40e00000, v158
	v_mul_f32_e32 v21, 0xc01d265f, v20
	v_exp_f32_e32 v21, v21
	v_mov_b32_e32 v241, v23
	v_min_f32_e32 v23, 0x40e00000, v159
	v_add_f32_e32 v21, 1.0, v21
	v_mul_f32_e32 v24, 0xc01d265f, v23
	v_rcp_f32_e32 v21, v21
	v_exp_f32_e32 v24, v24
	v_mul_f32_e32 v20, v20, v21
	v_med3_f32 v21, v126, s80, v206
	v_mul_f32_e32 v20, v21, v20
	v_add_f32_e32 v21, 1.0, v24
	v_rcp_f32_e32 v21, v21
	s_nop 0
	v_mul_f32_e32 v21, v23, v21
	v_mov_b32_e32 v23, v183
	v_cvt_pk_fp8_f32 v23, v18, v19
	v_med3_f32 v18, v127, s80, v206
	v_mul_f32_e32 v18, v18, v21
	v_cvt_pk_fp8_f32 v23, v20, v18 op_sel:[0,0,1]
	v_min_f32_e32 v20, 0x40e00000, v152
	v_mul_f32_e32 v18, 0xc01d265f, v20
	v_exp_f32_e32 v21, v18
	v_min_f32_e32 v24, 0x40e00000, v153
	v_mul_f32_e32 v25, 0xc01d265f, v24
	v_add_f32_e32 v21, 1.0, v21
	v_rcp_f32_e32 v21, v21
	v_exp_f32_e32 v25, v25
	v_mul_f32_e32 v20, v20, v21
	v_med3_f32 v21, v120, s80, v206
	v_mul_f32_e32 v20, v21, v20
	v_add_f32_e32 v21, 1.0, v25
	v_rcp_f32_e32 v21, v21
	v_med3_f32 v22, v121, s80, v206
	v_mul_f32_e32 v21, v24, v21
	v_mul_f32_e32 v21, v22, v21
	v_min_f32_e32 v22, 0x40e00000, v154
	v_mul_f32_e32 v24, 0xc01d265f, v22
	v_exp_f32_e32 v24, v24
	v_min_f32_e32 v26, 0x40e00000, v155
	v_mul_f32_e32 v27, 0xc01d265f, v26
	v_add_f32_e32 v24, 1.0, v24
	v_rcp_f32_e32 v24, v24
	v_exp_f32_e32 v27, v27
	v_mul_f32_e32 v22, v22, v24
	v_med3_f32 v24, v122, s80, v206
	v_mul_f32_e32 v22, v24, v22
	v_add_f32_e32 v24, 1.0, v27
	v_rcp_f32_e32 v24, v24
	v_med3_f32 v25, v123, s80, v206
	v_mul_f32_e32 v24, v26, v24
	v_mul_f32_e32 v24, v25, v24
	v_mov_b32_e32 v25, v183
	v_cvt_pk_fp8_f32 v25, v20, v21
	v_min_f32_e32 v20, 0x40e00000, v148
	v_mul_f32_e32 v21, 0xc01d265f, v20
	v_exp_f32_e32 v21, v21
	v_cvt_pk_fp8_f32 v25, v22, v24 op_sel:[0,0,1]
	v_min_f32_e32 v24, 0x40e00000, v149
	v_add_f32_e32 v21, 1.0, v21
	v_mul_f32_e32 v26, 0xc01d265f, v24
	v_rcp_f32_e32 v21, v21
	v_exp_f32_e32 v26, v26
	v_mul_f32_e32 v20, v20, v21
	v_med3_f32 v21, v116, s80, v206
	v_mul_f32_e32 v20, v21, v20
	v_add_f32_e32 v21, 1.0, v26
	v_rcp_f32_e32 v21, v21
	v_med3_f32 v22, v117, s80, v206
	v_mul_f32_e32 v21, v24, v21
	v_mul_f32_e32 v21, v22, v21
	v_min_f32_e32 v22, 0x40e00000, v150
	v_mul_f32_e32 v24, 0xc01d265f, v22
	v_exp_f32_e32 v24, v24
	v_min_f32_e32 v27, 0x40e00000, v151
	v_mul_f32_e32 v28, 0xc01d265f, v27
	v_add_f32_e32 v24, 1.0, v24
	v_rcp_f32_e32 v24, v24
	v_exp_f32_e32 v28, v28
	v_mul_f32_e32 v22, v22, v24
	v_med3_f32 v24, v118, s80, v206
	v_mul_f32_e32 v22, v24, v22
	v_add_f32_e32 v24, 1.0, v28
	v_rcp_f32_e32 v24, v24
	v_med3_f32 v26, v119, s80, v206
	v_mul_f32_e32 v24, v27, v24
	v_mul_f32_e32 v24, v26, v24
	v_mov_b32_e32 v26, v183
	v_cvt_pk_fp8_f32 v26, v20, v21
	v_min_f32_e32 v20, 0x40e00000, v144
	v_mul_f32_e32 v21, 0xc01d265f, v20
	v_exp_f32_e32 v21, v21
	v_cvt_pk_fp8_f32 v26, v22, v24 op_sel:[0,0,1]
	v_min_f32_e32 v24, 0x40e00000, v145
	v_add_f32_e32 v21, 1.0, v21
	v_mul_f32_e32 v27, 0xc01d265f, v24
	v_rcp_f32_e32 v21, v21
	v_exp_f32_e32 v27, v27
	v_mul_f32_e32 v20, v20, v21
	v_med3_f32 v21, v112, s80, v206
	v_mul_f32_e32 v20, v21, v20
	v_add_f32_e32 v21, 1.0, v27
	v_rcp_f32_e32 v21, v21
	v_med3_f32 v22, v113, s80, v206
	v_mul_f32_e32 v21, v24, v21
	v_mul_f32_e32 v21, v22, v21
	v_min_f32_e32 v22, 0x40e00000, v146
	v_mul_f32_e32 v24, 0xc01d265f, v22
	v_exp_f32_e32 v24, v24
	v_min_f32_e32 v28, 0x40e00000, v147
	v_mul_f32_e32 v29, 0xc01d265f, v28
	v_add_f32_e32 v24, 1.0, v24
	v_rcp_f32_e32 v24, v24
	v_exp_f32_e32 v29, v29
	v_mul_f32_e32 v22, v22, v24
	v_med3_f32 v24, v114, s80, v206
	v_mul_f32_e32 v22, v24, v22
	v_add_f32_e32 v24, 1.0, v29
	v_rcp_f32_e32 v24, v24
	s_nop 0
	v_mul_f32_e32 v24, v28, v24
	v_mov_b32_e32 v28, v183
	v_cvt_pk_fp8_f32 v28, v20, v21
	v_med3_f32 v20, v115, s80, v206
	v_mul_f32_e32 v20, v20, v24
	v_add_co_u32_e32 v18, vcc, s5, v16
	v_addc_co_u32_e32 v19, vcc, 0, v17, vcc
	v_cvt_pk_fp8_f32 v28, v22, v20 op_sel:[0,0,1]
	v_mov_b32_e32 v238, v23
	v_mov_b32_e32 v242, v25
	v_mov_b32_e32 v239, v26
	v_mov_b32_e32 v243, v28
	s_nop 1
	v_permlane32_swap_b32_e32 v236, v238
	v_permlane32_swap_b32_e32 v237, v239
	v_permlane32_swap_b32_e32 v240, v242
	v_permlane32_swap_b32_e32 v241, v243
	s_nop 0
	v_permlane16_swap_b32_e32 v236, v237
	v_permlane16_swap_b32_e32 v238, v239
	v_permlane16_swap_b32_e32 v240, v241
	v_permlane16_swap_b32_e32 v242, v243
	global_store_dwordx4 v[252:253], v[236:239], off
	global_store_dwordx4 v[252:253], v[240:243], off offset:16
	v_min_f32_e32 v20, 0x40e00000, v108
	v_mul_f32_e32 v18, 0xc01d265f, v20
	v_exp_f32_e32 v21, v18
	v_min_f32_e32 v23, 0x40e00000, v109
	v_mul_f32_e32 v24, 0xc01d265f, v23
	v_add_f32_e32 v21, 1.0, v21
	v_rcp_f32_e32 v21, v21
	v_exp_f32_e32 v24, v24
	v_mul_f32_e32 v20, v20, v21
	v_med3_f32 v21, v76, s80, v206
	v_mul_f32_e32 v20, v21, v20
	v_add_f32_e32 v21, 1.0, v24
	v_rcp_f32_e32 v21, v21
	v_med3_f32 v22, v77, s80, v206
	v_mul_f32_e32 v21, v23, v21
	v_mul_f32_e32 v21, v22, v21
	v_min_f32_e32 v22, 0x40e00000, v110
	v_mul_f32_e32 v23, 0xc01d265f, v22
	v_exp_f32_e32 v23, v23
	v_min_f32_e32 v25, 0x40e00000, v111
	v_mul_f32_e32 v26, 0xc01d265f, v25
	v_add_f32_e32 v23, 1.0, v23
	v_rcp_f32_e32 v23, v23
	v_exp_f32_e32 v26, v26
	v_mul_f32_e32 v22, v22, v23
	v_med3_f32 v23, v78, s80, v206
	v_mul_f32_e32 v22, v23, v22
	v_add_f32_e32 v23, 1.0, v26
	v_rcp_f32_e32 v23, v23
	s_nop 0
	v_mul_f32_e32 v23, v25, v23
	v_mov_b32_e32 v25, v183
	v_cvt_pk_fp8_f32 v25, v20, v21
	v_med3_f32 v20, v79, s80, v206
	v_mul_f32_e32 v20, v20, v23
	v_cvt_pk_fp8_f32 v25, v22, v20 op_sel:[0,0,1]
	v_min_f32_e32 v20, 0x40e00000, v104
	v_mul_f32_e32 v21, 0xc01d265f, v20
	v_exp_f32_e32 v21, v21
	v_min_f32_e32 v23, 0x40e00000, v105
	v_mul_f32_e32 v24, 0xc01d265f, v23
	v_add_f32_e32 v21, 1.0, v21
	v_rcp_f32_e32 v21, v21
	v_exp_f32_e32 v24, v24
	v_mul_f32_e32 v20, v20, v21
	v_med3_f32 v21, v72, s80, v206
	v_mul_f32_e32 v20, v21, v20
	v_add_f32_e32 v21, 1.0, v24
	v_rcp_f32_e32 v21, v21
	v_med3_f32 v22, v73, s80, v206
	v_mul_f32_e32 v21, v23, v21
	v_mul_f32_e32 v21, v22, v21
	v_min_f32_e32 v22, 0x40e00000, v106
	v_mul_f32_e32 v23, 0xc01d265f, v22
	s_mov_b32 s5, 0x41000
	v_lshl_add_u64 v[18:19], v[16:17], 0, s[26:27]
	v_add_co_u32_e32 v16, vcc, s5, v16
	v_exp_f32_e32 v23, v23
	s_nop 0
	v_addc_co_u32_e32 v17, vcc, 0, v17, vcc
	v_mov_b32_e32 v244, v25
	v_min_f32_e32 v25, 0x40e00000, v107
	v_add_f32_e32 v23, 1.0, v23
	v_mul_f32_e32 v26, 0xc01d265f, v25
	v_rcp_f32_e32 v23, v23
	v_exp_f32_e32 v26, v26
	v_mul_f32_e32 v22, v22, v23
	v_med3_f32 v23, v74, s80, v206
	v_mul_f32_e32 v22, v23, v22
	v_add_f32_e32 v23, 1.0, v26
	v_rcp_f32_e32 v23, v23
	s_nop 0
	v_mul_f32_e32 v23, v25, v23
	v_mov_b32_e32 v25, v183
	v_cvt_pk_fp8_f32 v25, v20, v21
	v_med3_f32 v20, v75, s80, v206
	v_mul_f32_e32 v20, v20, v23
	v_cvt_pk_fp8_f32 v25, v22, v20 op_sel:[0,0,1]
	v_min_f32_e32 v20, 0x40e00000, v100
	v_mul_f32_e32 v21, 0xc01d265f, v20
	v_exp_f32_e32 v21, v21
	v_min_f32_e32 v23, 0x40e00000, v101
	v_mul_f32_e32 v24, 0xc01d265f, v23
	v_add_f32_e32 v21, 1.0, v21
	v_rcp_f32_e32 v21, v21
	v_exp_f32_e32 v24, v24
	v_mul_f32_e32 v20, v20, v21
	v_med3_f32 v21, v68, s80, v206
	v_mul_f32_e32 v20, v21, v20
	v_add_f32_e32 v21, 1.0, v24
	v_rcp_f32_e32 v21, v21
	v_med3_f32 v22, v69, s80, v206
	v_mul_f32_e32 v21, v23, v21
	v_mul_f32_e32 v21, v22, v21
	v_min_f32_e32 v22, 0x40e00000, v102
	v_mul_f32_e32 v23, 0xc01d265f, v22
	v_exp_f32_e32 v23, v23
	v_mov_b32_e32 v236, v25
	v_min_f32_e32 v25, 0x40e00000, v103
	v_add_f32_e32 v23, 1.0, v23
	v_mul_f32_e32 v26, 0xc01d265f, v25
	v_rcp_f32_e32 v23, v23
	v_exp_f32_e32 v26, v26
	v_mul_f32_e32 v22, v22, v23
	v_med3_f32 v23, v70, s80, v206
	v_mul_f32_e32 v22, v23, v22
	v_add_f32_e32 v23, 1.0, v26
	v_rcp_f32_e32 v23, v23
	s_nop 0
	v_mul_f32_e32 v23, v25, v23
	v_mov_b32_e32 v25, v183
	v_cvt_pk_fp8_f32 v25, v20, v21
	v_med3_f32 v20, v71, s80, v206
	v_mul_f32_e32 v20, v20, v23
	v_cvt_pk_fp8_f32 v25, v22, v20 op_sel:[0,0,1]
	v_min_f32_e32 v20, 0x40e00000, v96
	v_mul_f32_e32 v21, 0xc01d265f, v20
	v_exp_f32_e32 v21, v21
	v_min_f32_e32 v23, 0x40e00000, v97
	v_mul_f32_e32 v24, 0xc01d265f, v23
	v_add_f32_e32 v21, 1.0, v21
	v_rcp_f32_e32 v21, v21
	v_exp_f32_e32 v24, v24
	v_mul_f32_e32 v20, v20, v21
	v_med3_f32 v21, v64, s80, v206
	v_mul_f32_e32 v20, v21, v20
	v_add_f32_e32 v21, 1.0, v24
	v_rcp_f32_e32 v21, v21
	v_med3_f32 v22, v65, s80, v206
	v_mul_f32_e32 v21, v23, v21
	v_mul_f32_e32 v21, v22, v21
	v_min_f32_e32 v22, 0x40e00000, v98
	v_mul_f32_e32 v23, 0xc01d265f, v22
	v_exp_f32_e32 v23, v23
	v_mov_b32_e32 v245, v25
	v_min_f32_e32 v25, 0x40e00000, v99
	v_add_f32_e32 v23, 1.0, v23
	v_mul_f32_e32 v26, 0xc01d265f, v25
	v_rcp_f32_e32 v23, v23
	v_exp_f32_e32 v26, v26
	v_mul_f32_e32 v22, v22, v23
	v_med3_f32 v23, v66, s80, v206
	v_mul_f32_e32 v22, v23, v22
	v_add_f32_e32 v23, 1.0, v26
	v_rcp_f32_e32 v23, v23
	s_nop 0
	v_mul_f32_e32 v23, v25, v23
	v_mov_b32_e32 v25, v183
	v_cvt_pk_fp8_f32 v25, v20, v21
	v_med3_f32 v20, v67, s80, v206
	v_mul_f32_e32 v20, v20, v23
	v_cvt_pk_fp8_f32 v25, v22, v20 op_sel:[0,0,1]
	v_min_f32_e32 v20, 0x40e00000, v92
	v_mul_f32_e32 v21, 0xc01d265f, v20
	v_exp_f32_e32 v21, v21
	v_mov_b32_e32 v237, v25
	v_med3_f32 v18, v60, s80, v206
	v_add_f32_e32 v19, 1.0, v21
	v_min_f32_e32 v21, 0x40e00000, v93
	v_mul_f32_e32 v22, 0xc01d265f, v21
	v_rcp_f32_e32 v19, v19
	v_exp_f32_e32 v22, v22
	v_mul_f32_e32 v19, v20, v19
	v_mul_f32_e32 v18, v18, v19
	v_add_f32_e32 v19, 1.0, v22
	v_rcp_f32_e32 v19, v19
	v_med3_f32 v20, v61, s80, v206
	v_mul_f32_e32 v19, v21, v19
	v_mul_f32_e32 v19, v20, v19
	v_min_f32_e32 v20, 0x40e00000, v94
	v_mul_f32_e32 v21, 0xc01d265f, v20
	v_exp_f32_e32 v21, v21
	v_min_f32_e32 v23, 0x40e00000, v95
	v_mul_f32_e32 v24, 0xc01d265f, v23
	v_add_f32_e32 v21, 1.0, v21
	v_rcp_f32_e32 v21, v21
	v_exp_f32_e32 v24, v24
	v_mul_f32_e32 v20, v20, v21
	v_med3_f32 v21, v62, s80, v206
	v_mul_f32_e32 v20, v21, v20
	v_add_f32_e32 v21, 1.0, v24
	v_rcp_f32_e32 v21, v21
	s_nop 0
	v_mul_f32_e32 v21, v23, v21
	v_mov_b32_e32 v23, v183
	v_cvt_pk_fp8_f32 v23, v18, v19
	v_med3_f32 v18, v63, s80, v206
	v_mul_f32_e32 v18, v18, v21
	v_cvt_pk_fp8_f32 v23, v20, v18 op_sel:[0,0,1]
	v_min_f32_e32 v18, 0x40e00000, v88
	v_mul_f32_e32 v19, 0xc01d265f, v18
	v_exp_f32_e32 v19, v19
	v_min_f32_e32 v21, 0x40e00000, v89
	v_mul_f32_e32 v22, 0xc01d265f, v21
	v_add_f32_e32 v19, 1.0, v19
	v_rcp_f32_e32 v19, v19
	v_exp_f32_e32 v22, v22
	v_mul_f32_e32 v18, v18, v19
	v_med3_f32 v19, v56, s80, v206
	v_mul_f32_e32 v18, v19, v18
	v_add_f32_e32 v19, 1.0, v22
	v_rcp_f32_e32 v19, v19
	v_med3_f32 v20, v57, s80, v206
	v_mul_f32_e32 v19, v21, v19
	v_mul_f32_e32 v19, v20, v19
	v_min_f32_e32 v20, 0x40e00000, v90
	v_mul_f32_e32 v21, 0xc01d265f, v20
	v_exp_f32_e32 v21, v21
	v_mov_b32_e32 v246, v23
	v_min_f32_e32 v23, 0x40e00000, v91
	v_add_f32_e32 v21, 1.0, v21
	v_mul_f32_e32 v24, 0xc01d265f, v23
	v_rcp_f32_e32 v21, v21
	v_exp_f32_e32 v24, v24
	v_mul_f32_e32 v20, v20, v21
	v_med3_f32 v21, v58, s80, v206
	v_mul_f32_e32 v20, v21, v20
	v_add_f32_e32 v21, 1.0, v24
	v_rcp_f32_e32 v21, v21
	s_nop 0
	v_mul_f32_e32 v21, v23, v21
	v_mov_b32_e32 v23, v183
	v_cvt_pk_fp8_f32 v23, v18, v19
	v_med3_f32 v18, v59, s80, v206
	v_mul_f32_e32 v18, v18, v21
	v_min_f32_e32 v8, 0x40e00000, v84
	v_cvt_pk_fp8_f32 v23, v20, v18 op_sel:[0,0,1]
	v_mul_f32_e32 v18, 0xc01d265f, v8
	v_exp_f32_e32 v18, v18
	v_min_f32_e32 v9, 0x40e00000, v85
	v_mul_f32_e32 v19, 0xc01d265f, v9
	v_add_f32_e32 v18, 1.0, v18
	v_rcp_f32_e32 v18, v18
	v_exp_f32_e32 v19, v19
	v_med3_f32 v12, v52, s80, v206
	v_mul_f32_e32 v8, v8, v18
	v_mul_f32_e32 v8, v12, v8
	v_add_f32_e32 v12, 1.0, v19
	v_rcp_f32_e32 v12, v12
	s_nop 0
	v_mul_f32_e32 v9, v9, v12
	v_med3_f32 v12, v53, s80, v206
	v_min_f32_e32 v10, 0x40e00000, v86
	v_mul_f32_e32 v9, v12, v9
	v_mul_f32_e32 v12, 0xc01d265f, v10
	v_exp_f32_e32 v12, v12
	v_min_f32_e32 v11, 0x40e00000, v87
	v_add_f32_e32 v12, 1.0, v12
	v_mul_f32_e32 v14, 0xc01d265f, v11
	v_rcp_f32_e32 v12, v12
	v_exp_f32_e32 v14, v14
	v_mul_f32_e32 v10, v10, v12
	v_med3_f32 v12, v54, s80, v206
	v_mul_f32_e32 v10, v12, v10
	v_add_f32_e32 v12, 1.0, v14
	v_rcp_f32_e32 v12, v12
	s_nop 0
	v_mul_f32_e32 v11, v11, v12
	v_mov_b32_e32 v12, v183
	v_cvt_pk_fp8_f32 v12, v8, v9
	v_med3_f32 v8, v55, s80, v206
	v_mul_f32_e32 v8, v8, v11
	v_min_f32_e32 v4, 0x40e00000, v80
	v_cvt_pk_fp8_f32 v12, v10, v8 op_sel:[0,0,1]
	v_mul_f32_e32 v8, 0xc01d265f, v4
	v_exp_f32_e32 v8, v8
	v_min_f32_e32 v5, 0x40e00000, v81
	v_mul_f32_e32 v9, 0xc01d265f, v5
	v_add_f32_e32 v8, 1.0, v8
	v_rcp_f32_e32 v8, v8
	v_exp_f32_e32 v9, v9
	v_med3_f32 v0, v48, s80, v206
	v_mul_f32_e32 v4, v4, v8
	v_mul_f32_e32 v0, v0, v4
	v_add_f32_e32 v4, 1.0, v9
	v_rcp_f32_e32 v4, v4
	v_med3_f32 v1, v49, s80, v206
	v_mul_f32_e32 v4, v5, v4
	v_mul_f32_e32 v1, v1, v4
	v_min_f32_e32 v4, 0x40e00000, v82
	v_mul_f32_e32 v5, 0xc01d265f, v4
	v_exp_f32_e32 v5, v5
	v_min_f32_e32 v6, 0x40e00000, v83
	v_mul_f32_e32 v7, 0xc01d265f, v6
	v_add_f32_e32 v5, 1.0, v5
	v_rcp_f32_e32 v5, v5
	v_exp_f32_e32 v7, v7
	v_med3_f32 v2, v50, s80, v206
	v_mul_f32_e32 v4, v4, v5
	v_mul_f32_e32 v2, v2, v4
	v_add_f32_e32 v4, 1.0, v7
	v_rcp_f32_e32 v4, v4
	v_mov_b32_e32 v5, v183
	v_cvt_pk_fp8_f32 v5, v0, v1
	v_mul_f32_e32 v4, v6, v4
	v_med3_f32 v0, v51, s80, v206
	v_mul_f32_e32 v0, v0, v4
	v_cvt_pk_fp8_f32 v5, v2, v0 op_sel:[0,0,1]
	s_andn2_b64 vcc, exec, s[24:25]
	v_mov_b32_e32 v238, v23
	v_mov_b32_e32 v247, v12
	v_mov_b32_e32 v239, v5
	s_nop 1
	v_permlane32_swap_b32_e32 v244, v246
	v_permlane32_swap_b32_e32 v245, v247
	v_permlane32_swap_b32_e32 v236, v238
	v_permlane32_swap_b32_e32 v237, v239
	s_nop 0
	v_permlane16_swap_b32_e32 v244, v245
	v_permlane16_swap_b32_e32 v246, v247
	v_permlane16_swap_b32_e32 v236, v237
	v_permlane16_swap_b32_e32 v238, v239
	global_store_dwordx4 v[254:255], v[244:247], off
	global_store_dwordx4 v[254:255], v[236:239], off offset:16
	s_cbranch_vccnz .LBB0_784
	s_mov_b32 s71, s44
	s_mov_b32 s8, s22
	s_mov_b64 s[6:7], s[20:21]
	s_mov_b32 s4, s18
	s_mov_b32 s45, s72
	s_mov_b32 s10, s19
	s_mov_b32 s76, s52
	s_waitcnt vmcnt(4)
	v_add_f32_e32 v140, 1.0, v140
	v_add_f32_e32 v141, 1.0, v141
	v_add_f32_e32 v142, 1.0, v142
	v_add_f32_e32 v143, 1.0, v143
	v_add_f32_e32 v136, 1.0, v136
	v_add_f32_e32 v137, 1.0, v137
	v_add_f32_e32 v138, 1.0, v138
	v_add_f32_e32 v139, 1.0, v139
	v_mov_b64_e32 v[164:165], v[172:173]
	v_mov_b64_e32 v[166:167], v[174:175]
	v_mov_b64_e32 v[160:161], v[168:169]
	v_mov_b64_e32 v[162:163], v[170:171]
	v_mov_b64_e32 v[156:157], v[172:173]
	v_mov_b64_e32 v[158:159], v[174:175]
	v_mov_b64_e32 v[152:153], v[168:169]
	v_mov_b64_e32 v[154:155], v[170:171]
	v_mov_b64_e32 v[148:149], v[172:173]
	v_mov_b64_e32 v[150:151], v[174:175]
	v_mov_b64_e32 v[144:145], v[168:169]
	v_mov_b64_e32 v[146:147], v[170:171]
	v_mov_b64_e32 v[132:133], v[140:141]
	v_mov_b64_e32 v[134:135], v[142:143]
	v_mov_b64_e32 v[128:129], v[136:137]
	v_mov_b64_e32 v[130:131], v[138:139]
	v_mov_b64_e32 v[124:125], v[140:141]
	v_mov_b64_e32 v[126:127], v[142:143]
	v_mov_b64_e32 v[120:121], v[136:137]
	v_mov_b64_e32 v[122:123], v[138:139]
	v_mov_b64_e32 v[116:117], v[140:141]
	v_mov_b64_e32 v[118:119], v[142:143]
	v_mov_b64_e32 v[112:113], v[136:137]
	v_mov_b64_e32 v[114:115], v[138:139]
	v_mov_b64_e32 v[108:109], v[172:173]
	v_mov_b64_e32 v[110:111], v[174:175]
	v_mov_b64_e32 v[104:105], v[168:169]
	v_mov_b64_e32 v[106:107], v[170:171]
	v_mov_b64_e32 v[100:101], v[172:173]
	v_mov_b64_e32 v[102:103], v[174:175]
	v_mov_b64_e32 v[96:97], v[168:169]
	v_mov_b64_e32 v[98:99], v[170:171]
	v_mov_b64_e32 v[92:93], v[172:173]
	v_mov_b64_e32 v[94:95], v[174:175]
	v_mov_b64_e32 v[88:89], v[168:169]
	v_mov_b64_e32 v[90:91], v[170:171]
	v_mov_b64_e32 v[84:85], v[172:173]
	v_mov_b64_e32 v[86:87], v[174:175]
	v_mov_b64_e32 v[80:81], v[168:169]
	v_mov_b64_e32 v[82:83], v[170:171]
	v_mov_b64_e32 v[76:77], v[140:141]
	v_mov_b64_e32 v[78:79], v[142:143]
	v_mov_b64_e32 v[72:73], v[136:137]
	v_mov_b64_e32 v[74:75], v[138:139]
	v_mov_b64_e32 v[68:69], v[140:141]
	v_mov_b64_e32 v[70:71], v[142:143]
	v_mov_b64_e32 v[64:65], v[136:137]
	v_mov_b64_e32 v[66:67], v[138:139]
	v_mov_b64_e32 v[60:61], v[140:141]
	v_mov_b64_e32 v[62:63], v[142:143]
	v_mov_b64_e32 v[56:57], v[136:137]
	v_mov_b64_e32 v[58:59], v[138:139]
	v_mov_b64_e32 v[52:53], v[140:141]
	v_mov_b64_e32 v[54:55], v[142:143]
	v_mov_b64_e32 v[48:49], v[136:137]
	v_mov_b64_e32 v[50:51], v[138:139]
	s_branch .LBB0_784

.LBB0_993:
	v_bfe_u32 v2, v178, 4, 2
	v_and_b32_e32 v0, 15, v178
	v_lshlrev_b32_e32 v1, 4, v2
	v_lshlrev_b32_e32 v3, 2, v178
	v_lshl_or_b32 v193, s11, 6, v0
	v_lshl_or_b32 v0, v0, 6, v1
	s_lshl_b32 s11, s11, 13
	v_and_b32_e32 v3, 32, v3
	v_bitop3_b32 v194, v0, s11, v3 bitop3:0xde
	s_lshl_b32 s11, s14, 5
	s_and_b32 s14, s11, 0x60
	v_lshlrev_b32_e32 v0, 6, v178
	s_movk_i32 s11, 0x3c0
	v_and_or_b32 v0, v0, s11, v1
	s_lshl_b32 s11, s14, 7
	s_add_u32 s16, s90, 0x191a0000
	s_addc_u32 s17, s91, 0
	s_add_u32 s18, s8, 0x4000
	s_addc_u32 s19, s9, 0
	s_add_i32 s52, s46, 0x8000
	v_bitop3_b32 v3, s11, v0, v3 bitop3:0xf6
	v_lshl_add_u64 v[0:1], s[18:19], 0, v[176:177]
	s_mov_b32 m0, s52
	s_add_i32 s53, s46, 0xa000
	s_waitcnt vmcnt(4)
	s_barrier
	global_load_lds_dwordx4 v[0:1], off
	v_lshl_add_u64 v[0:1], s[18:19], 0, v[180:181]
	s_add_u32 s18, s90, 0xf1a4000
	s_mov_b32 m0, s53
	s_addc_u32 s19, s91, 0
	global_load_lds_dwordx4 v[0:1], off
	s_add_i32 m0, s46, 0x18000
	v_lshl_add_u64 v[0:1], s[18:19], 0, v[184:185]
	global_load_lds_dwordx4 v[0:1], off
	s_add_i32 m0, s46, 0x1a000
	v_lshl_add_u64 v[0:1], s[18:19], 0, v[186:187]
	s_add_u32 s18, s8, 0x5000
	s_addc_u32 s19, s9, 0
	s_add_i32 s54, s46, 0xc000
	global_load_lds_dwordx4 v[0:1], off
	v_lshl_add_u64 v[0:1], s[18:19], 0, v[176:177]
	s_mov_b32 m0, s54
	s_add_i32 s55, s46, 0xe000
	global_load_lds_dwordx4 v[0:1], off
	v_lshl_add_u64 v[0:1], s[18:19], 0, v[180:181]
	s_mov_b32 m0, s55
	s_ashr_i32 s18, s33, 31
	global_load_lds_dwordx4 v[0:1], off
	s_lshr_b32 s18, s18, 29
	s_add_i32 s18, s33, s18
	s_ashr_i32 s19, s18, 3
	s_and_b32 s18, s18, -8
	s_sub_i32 s18, s33, s18
	s_ashr_i32 s20, s96, 3
	s_mul_i32 s18, s20, s18
	s_add_i32 s20, s18, s19
	s_cmp_lt_i32 s36, 24
	s_cselect_b64 s[18:19], -1, 0
	s_and_b64 s[2:3], s[2:3], exec
	s_mov_b32 s2, 0x20944
	s_cselect_b32 s56, s20, s33
	s_add_i32 s57, s2, 0x100
	s_mov_b32 s2, 0x20948
	s_add_i32 s58, s2, 0x100
	s_mov_b32 s2, 0x2094c
	s_add_i32 s59, s2, 0x100
	s_mov_b32 s2, 0x20950
	s_add_i32 s60, s2, 0x100
	s_mov_b32 s2, 0x20954
	s_add_i32 s61, s2, 0x100
	s_mov_b32 s2, 0x20958
	s_add_i32 s62, s2, 0x100
	s_mov_b32 s2, 0x2095c
	s_add_i32 s63, s2, 0x100
	s_mov_b32 s2, 0x20960
	s_add_i32 s64, s2, 0x100
	s_mov_b32 s2, 0x20964
	s_add_i32 s65, s2, 0x100
	s_mov_b32 s2, 0x20968
	s_add_i32 s68, s2, 0x100
	s_mov_b32 s2, 0x2096c
	s_add_i32 s69, s2, 0x100
	s_mov_b32 s2, 0x20970
	s_add_i32 s70, s2, 0x100
	s_mov_b32 s2, 0x20974
	s_addk_i32 s2, 0x100
	v_writelane_b32 v250, s2, 4
	s_mov_b32 s2, 0x20978
	s_addk_i32 s2, 0x100
	v_writelane_b32 v250, s2, 3
	s_mov_b32 s2, 0x2097c
	s_addk_i32 s2, 0x100
	v_writelane_b32 v250, s2, 5
	s_mov_b32 s2, 0x20980
	s_addk_i32 s2, 0x100
	v_writelane_b32 v250, s2, 6
	s_mov_b32 s2, 0x20984
	s_addk_i32 s2, 0x100
	v_writelane_b32 v250, s2, 7
	s_mov_b32 s2, 0x20988
	s_addk_i32 s2, 0x100
	v_writelane_b32 v250, s2, 8
	s_mov_b32 s2, 0x2098c
	s_addk_i32 s2, 0x100
	v_writelane_b32 v250, s2, 9
	s_mov_b32 s2, 0x20990
	s_addk_i32 s2, 0x100
	v_writelane_b32 v250, s2, 10
	s_mov_b32 s2, 0x20994
	s_addk_i32 s2, 0x100
	v_writelane_b32 v250, s2, 11
	s_mov_b32 s2, 0x20998
	s_addk_i32 s2, 0x100
	v_writelane_b32 v250, s2, 12
	s_mov_b32 s2, 0x2099c
	s_addk_i32 s2, 0x100
	v_writelane_b32 v250, s2, 13
	s_mov_b32 s2, 0x209a0
	s_addk_i32 s2, 0x100
	v_writelane_b32 v250, s2, 14
	s_mov_b32 s2, 0x209a4
	s_addk_i32 s2, 0x100
	v_writelane_b32 v250, s2, 15
	s_mov_b32 s2, 0x209a8
	s_add_i32 s84, s2, 0x100
	s_mov_b32 s2, 0x209ac
	s_add_i32 s85, s2, 0x100
	s_mov_b32 s2, 0x209b0
	s_add_i32 s97, s2, 0x100
	s_mov_b32 s2, 0x209b4
	s_waitcnt vmcnt(6)
	s_add_i32 s74, s2, 0x100
	s_mov_b32 s2, 0x209b8
	s_mov_b32 s11, 0x18000
	s_mov_b32 s15, 0
	v_lshlrev_b32_e32 v190, 2, v2
	s_add_i32 s73, s2, 0x100
	s_mov_b32 s2, 0x209bc
	v_mov_b32_e32 v191, v183
	v_or_b32_e32 v185, 16, v193
	v_or_b32_e32 v187, 32, v193
	v_or_b32_e32 v195, 48, v193
	s_add_i32 s75, s2, 0x100
	v_mov_b32_e32 v196, 0x7f7f7f7f
	v_mov_b32_e32 v197, 0x79797979
	s_add_i32 s76, s7, 0x100
	s_lshl_b32 s72, s14, 2
	v_lshlrev_b32_e32 v198, 2, v190
	s_mov_b32 s77, 0xc3e00000
	v_add_u32_e32 v199, 0x100, v3
	s_add_i32 s78, s11, 0x100
	v_mov_b32_e32 v200, 0x43e00000
	s_mov_b32 s44, s81
	s_mov_b32 s80, s15
	s_lshl_b32 s99, s6, 13
	s_lshl_b32 s100, s10, 2
	s_add_u32 s99, s99, s100
	s_add_u32 s99, s99, s72
	s_add_u32 s99, s99, s72
	s_add_u32 s100, s86, s99
	s_addc_u32 s101, s87, 0
	global_load_dwordx4 v[172:175], v198, s[100:101]
	global_load_dwordx4 v[168:171], v198, s[100:101] offset:64
	global_load_dwordx4 v[140:143], v198, s[100:101] offset:128
	global_load_dwordx4 v[136:139], v198, s[100:101] offset:192
	s_waitcnt vmcnt(0)
	v_mov_b64_e32 v[164:165], v[172:173]
	v_mov_b64_e32 v[166:167], v[174:175]
	v_mov_b64_e32 v[160:161], v[168:169]
	v_mov_b64_e32 v[162:163], v[170:171]
	v_mov_b64_e32 v[156:157], v[172:173]
	v_mov_b64_e32 v[158:159], v[174:175]
	v_mov_b64_e32 v[152:153], v[168:169]
	v_mov_b64_e32 v[154:155], v[170:171]
	v_mov_b64_e32 v[148:149], v[172:173]
	v_mov_b64_e32 v[150:151], v[174:175]
	v_mov_b64_e32 v[144:145], v[168:169]
	v_mov_b64_e32 v[146:147], v[170:171]
	v_mov_b64_e32 v[132:133], v[140:141]
	v_mov_b64_e32 v[134:135], v[142:143]
	v_mov_b64_e32 v[128:129], v[136:137]
	v_mov_b64_e32 v[130:131], v[138:139]
	v_mov_b64_e32 v[124:125], v[140:141]
	v_mov_b64_e32 v[126:127], v[142:143]
	v_mov_b64_e32 v[120:121], v[136:137]
	v_mov_b64_e32 v[122:123], v[138:139]
	v_mov_b64_e32 v[116:117], v[140:141]
	v_mov_b64_e32 v[118:119], v[142:143]
	v_mov_b64_e32 v[112:113], v[136:137]
	v_mov_b64_e32 v[114:115], v[138:139]
	v_mov_b64_e32 v[108:109], v[172:173]
	v_mov_b64_e32 v[110:111], v[174:175]
	v_mov_b64_e32 v[104:105], v[168:169]
	v_mov_b64_e32 v[106:107], v[170:171]
	v_mov_b64_e32 v[100:101], v[172:173]
	v_mov_b64_e32 v[102:103], v[174:175]
	v_mov_b64_e32 v[96:97], v[168:169]
	v_mov_b64_e32 v[98:99], v[170:171]
	v_mov_b64_e32 v[92:93], v[172:173]
	v_mov_b64_e32 v[94:95], v[174:175]
	v_mov_b64_e32 v[88:89], v[168:169]
	v_mov_b64_e32 v[90:91], v[170:171]
	v_mov_b64_e32 v[84:85], v[172:173]
	v_mov_b64_e32 v[86:87], v[174:175]
	v_mov_b64_e32 v[80:81], v[168:169]
	v_mov_b64_e32 v[82:83], v[170:171]
	v_mov_b64_e32 v[76:77], v[140:141]
	v_mov_b64_e32 v[78:79], v[142:143]
	v_mov_b64_e32 v[72:73], v[136:137]
	v_mov_b64_e32 v[74:75], v[138:139]
	v_mov_b64_e32 v[68:69], v[140:141]
	v_mov_b64_e32 v[70:71], v[142:143]
	v_mov_b64_e32 v[64:65], v[136:137]
	v_mov_b64_e32 v[66:67], v[138:139]
	v_mov_b64_e32 v[60:61], v[140:141]
	v_mov_b64_e32 v[62:63], v[142:143]
	v_mov_b64_e32 v[56:57], v[136:137]
	v_mov_b64_e32 v[58:59], v[138:139]
	v_mov_b64_e32 v[52:53], v[140:141]
	v_mov_b64_e32 v[54:55], v[142:143]
	v_mov_b64_e32 v[48:49], v[136:137]
	v_mov_b64_e32 v[50:51], v[138:139]
	s_barrier
	s_branch .LBB0_995

.LBB0_1047:
	s_andn2_b64 vcc, exec, s[24:25]
	s_ashr_i32 s11, s10, 31
	v_add_u32_e32 v16, s44, v193
	v_ashrrev_i32_e32 v17, 31, v16
	v_lshlrev_b64 v[252:253], 11, v[16:17]
	v_bfe_u32 v16, v178, 4, 2
	v_lshlrev_b32_e32 v16, 4, v16
	v_mov_b32_e32 v17, 0
	v_lshl_add_u64 v[252:253], s[16:17], 0, v[252:253]
	v_lshl_add_u64 v[252:253], v[252:253], 0, s[10:11]
	v_lshl_add_u64 v[252:253], v[252:253], 0, s[14:15]
	v_lshl_add_u64 v[252:253], v[252:253], 0, s[14:15]
	v_lshl_add_u64 v[252:253], v[252:253], 0, v[16:17]
	s_mov_b64 s[100:101], 0x8000
	v_med3_f32 v24, v172, s77, v200
	v_med3_f32 v25, v173, s77, v200
	v_med3_f32 v26, v174, s77, v200
	v_med3_f32 v27, v175, s77, v200
	v_med3_f32 v28, v168, s77, v200
	v_med3_f32 v29, v169, s77, v200
	v_med3_f32 v30, v170, s77, v200
	v_med3_f32 v31, v171, s77, v200
	v_med3_f32 v32, v140, s77, v200
	v_med3_f32 v33, v141, s77, v200
	v_med3_f32 v34, v142, s77, v200
	v_med3_f32 v35, v143, s77, v200
	v_med3_f32 v36, v136, s77, v200
	v_med3_f32 v37, v137, s77, v200
	v_med3_f32 v38, v138, s77, v200
	v_med3_f32 v39, v139, s77, v200
	s_lshl_b32 s99, s20, 13
	s_lshl_b32 s100, s21, 2
	s_add_u32 s99, s99, s100
	s_add_u32 s99, s99, s72
	s_add_u32 s99, s99, s72
	s_add_u32 s100, s86, s99
	s_addc_u32 s101, s87, 0
	global_load_dwordx4 v[172:175], v198, s[100:101]
	global_load_dwordx4 v[168:171], v198, s[100:101] offset:64
	global_load_dwordx4 v[140:143], v198, s[100:101] offset:128
	global_load_dwordx4 v[136:139], v198, s[100:101] offset:192
	s_mov_b64 s[100:101], 0x8000
	v_cvt_pk_fp8_f32 v20, v24, v25
	v_cvt_pk_fp8_f32 v21, v28, v29
	v_cvt_pk_fp8_f32 v22, v32, v33
	v_cvt_pk_fp8_f32 v23, v36, v37
	v_cvt_pk_fp8_f32 v20, v26, v27 op_sel:[0,0,1]
	v_cvt_pk_fp8_f32 v21, v30, v31 op_sel:[0,0,1]
	v_cvt_pk_fp8_f32 v22, v34, v35 op_sel:[0,0,1]
	v_cvt_pk_fp8_f32 v23, v38, v39 op_sel:[0,0,1]
	s_nop 1
	v_permlane32_swap_b32_e32 v20, v22
	v_permlane32_swap_b32_e32 v21, v23
	s_nop 1
	v_permlane16_swap_b32_e32 v20, v21
	v_permlane16_swap_b32_e32 v22, v23
	global_store_dwordx4 v[252:253], v[20:23], off
	v_lshl_add_u64 v[252:253], v[252:253], 0, s[100:101]
	v_med3_f32 v24, v164, s77, v200
	v_med3_f32 v25, v165, s77, v200
	v_med3_f32 v26, v166, s77, v200
	v_med3_f32 v27, v167, s77, v200
	v_med3_f32 v28, v160, s77, v200
	v_med3_f32 v29, v161, s77, v200
	v_med3_f32 v30, v162, s77, v200
	v_med3_f32 v31, v163, s77, v200
	v_med3_f32 v32, v132, s77, v200
	v_med3_f32 v33, v133, s77, v200
	v_med3_f32 v34, v134, s77, v200
	v_med3_f32 v35, v135, s77, v200
	v_med3_f32 v36, v128, s77, v200
	v_med3_f32 v37, v129, s77, v200
	v_med3_f32 v38, v130, s77, v200
	v_med3_f32 v39, v131, s77, v200
	v_cvt_pk_fp8_f32 v40, v24, v25
	v_cvt_pk_fp8_f32 v41, v28, v29
	v_cvt_pk_fp8_f32 v42, v32, v33
	v_cvt_pk_fp8_f32 v43, v36, v37
	v_cvt_pk_fp8_f32 v40, v26, v27 op_sel:[0,0,1]
	v_cvt_pk_fp8_f32 v41, v30, v31 op_sel:[0,0,1]
	v_cvt_pk_fp8_f32 v42, v34, v35 op_sel:[0,0,1]
	v_cvt_pk_fp8_f32 v43, v38, v39 op_sel:[0,0,1]
	s_nop 1
	v_permlane32_swap_b32_e32 v40, v42
	v_permlane32_swap_b32_e32 v41, v43
	s_nop 1
	v_permlane16_swap_b32_e32 v40, v41
	v_permlane16_swap_b32_e32 v42, v43
	global_store_dwordx4 v[252:253], v[40:43], off
	v_lshl_add_u64 v[252:253], v[252:253], 0, s[100:101]
	v_med3_f32 v24, v156, s77, v200
	v_med3_f32 v25, v157, s77, v200
	v_med3_f32 v26, v158, s77, v200
	v_med3_f32 v27, v159, s77, v200
	v_med3_f32 v28, v152, s77, v200
	v_med3_f32 v29, v153, s77, v200
	v_med3_f32 v30, v154, s77, v200
	v_med3_f32 v31, v155, s77, v200
	v_med3_f32 v32, v124, s77, v200
	v_med3_f32 v33, v125, s77, v200
	v_med3_f32 v34, v126, s77, v200
	v_med3_f32 v35, v127, s77, v200
	v_med3_f32 v36, v120, s77, v200
	v_med3_f32 v37, v121, s77, v200
	v_med3_f32 v38, v122, s77, v200
	v_med3_f32 v39, v123, s77, v200
	v_cvt_pk_fp8_f32 v20, v24, v25
	v_cvt_pk_fp8_f32 v21, v28, v29
	v_cvt_pk_fp8_f32 v22, v32, v33
	v_cvt_pk_fp8_f32 v23, v36, v37
	v_cvt_pk_fp8_f32 v20, v26, v27 op_sel:[0,0,1]
	v_cvt_pk_fp8_f32 v21, v30, v31 op_sel:[0,0,1]
	v_cvt_pk_fp8_f32 v22, v34, v35 op_sel:[0,0,1]
	v_cvt_pk_fp8_f32 v23, v38, v39 op_sel:[0,0,1]
	s_nop 1
	v_permlane32_swap_b32_e32 v20, v22
	v_permlane32_swap_b32_e32 v21, v23
	s_nop 1
	v_permlane16_swap_b32_e32 v20, v21
	v_permlane16_swap_b32_e32 v22, v23
	global_store_dwordx4 v[252:253], v[20:23], off
	v_lshl_add_u64 v[252:253], v[252:253], 0, s[100:101]
	v_med3_f32 v24, v148, s77, v200
	v_med3_f32 v25, v149, s77, v200
	v_med3_f32 v26, v150, s77, v200
	v_med3_f32 v27, v151, s77, v200
	v_med3_f32 v28, v144, s77, v200
	v_med3_f32 v29, v145, s77, v200
	v_med3_f32 v30, v146, s77, v200
	v_med3_f32 v31, v147, s77, v200
	v_med3_f32 v32, v116, s77, v200
	v_med3_f32 v33, v117, s77, v200
	v_med3_f32 v34, v118, s77, v200
	v_med3_f32 v35, v119, s77, v200
	v_med3_f32 v36, v112, s77, v200
	v_med3_f32 v37, v113, s77, v200
	v_med3_f32 v38, v114, s77, v200
	v_med3_f32 v39, v115, s77, v200
	v_cvt_pk_fp8_f32 v40, v24, v25
	v_cvt_pk_fp8_f32 v41, v28, v29
	v_cvt_pk_fp8_f32 v42, v32, v33
	v_cvt_pk_fp8_f32 v43, v36, v37
	v_cvt_pk_fp8_f32 v40, v26, v27 op_sel:[0,0,1]
	v_cvt_pk_fp8_f32 v41, v30, v31 op_sel:[0,0,1]
	v_cvt_pk_fp8_f32 v42, v34, v35 op_sel:[0,0,1]
	v_cvt_pk_fp8_f32 v43, v38, v39 op_sel:[0,0,1]
	s_nop 1
	v_permlane32_swap_b32_e32 v40, v42
	v_permlane32_swap_b32_e32 v41, v43
	s_nop 1
	v_permlane16_swap_b32_e32 v40, v41
	v_permlane16_swap_b32_e32 v42, v43
	global_store_dwordx4 v[252:253], v[40:43], off
	s_mov_b64 s[100:101], 0x28000
	v_lshl_add_u64 v[252:253], v[252:253], 0, s[100:101]
	s_mov_b64 s[100:101], 0x8000
	v_med3_f32 v24, v108, s77, v200
	v_med3_f32 v25, v109, s77, v200
	v_med3_f32 v26, v110, s77, v200
	v_med3_f32 v27, v111, s77, v200
	v_med3_f32 v28, v104, s77, v200
	v_med3_f32 v29, v105, s77, v200
	v_med3_f32 v30, v106, s77, v200
	v_med3_f32 v31, v107, s77, v200
	v_med3_f32 v32, v76, s77, v200
	v_med3_f32 v33, v77, s77, v200
	v_med3_f32 v34, v78, s77, v200
	v_med3_f32 v35, v79, s77, v200
	v_med3_f32 v36, v72, s77, v200
	v_med3_f32 v37, v73, s77, v200
	v_med3_f32 v38, v74, s77, v200
	v_med3_f32 v39, v75, s77, v200
	v_cvt_pk_fp8_f32 v20, v24, v25
	v_cvt_pk_fp8_f32 v21, v28, v29
	v_cvt_pk_fp8_f32 v22, v32, v33
	v_cvt_pk_fp8_f32 v23, v36, v37
	v_cvt_pk_fp8_f32 v20, v26, v27 op_sel:[0,0,1]
	v_cvt_pk_fp8_f32 v21, v30, v31 op_sel:[0,0,1]
	v_cvt_pk_fp8_f32 v22, v34, v35 op_sel:[0,0,1]
	v_cvt_pk_fp8_f32 v23, v38, v39 op_sel:[0,0,1]
	s_nop 1
	v_permlane32_swap_b32_e32 v20, v22
	v_permlane32_swap_b32_e32 v21, v23
	s_nop 1
	v_permlane16_swap_b32_e32 v20, v21
	v_permlane16_swap_b32_e32 v22, v23
	global_store_dwordx4 v[252:253], v[20:23], off
	v_lshl_add_u64 v[252:253], v[252:253], 0, s[100:101]
	v_med3_f32 v24, v100, s77, v200
	v_med3_f32 v25, v101, s77, v200
	v_med3_f32 v26, v102, s77, v200
	v_med3_f32 v27, v103, s77, v200
	v_med3_f32 v28, v96, s77, v200
	v_med3_f32 v29, v97, s77, v200
	v_med3_f32 v30, v98, s77, v200
	v_med3_f32 v31, v99, s77, v200
	v_med3_f32 v32, v68, s77, v200
	v_med3_f32 v33, v69, s77, v200
	v_med3_f32 v34, v70, s77, v200
	v_med3_f32 v35, v71, s77, v200
	v_med3_f32 v36, v64, s77, v200
	v_med3_f32 v37, v65, s77, v200
	v_med3_f32 v38, v66, s77, v200
	v_med3_f32 v39, v67, s77, v200
	v_cvt_pk_fp8_f32 v40, v24, v25
	v_cvt_pk_fp8_f32 v41, v28, v29
	v_cvt_pk_fp8_f32 v42, v32, v33
	v_cvt_pk_fp8_f32 v43, v36, v37
	v_cvt_pk_fp8_f32 v40, v26, v27 op_sel:[0,0,1]
	v_cvt_pk_fp8_f32 v41, v30, v31 op_sel:[0,0,1]
	v_cvt_pk_fp8_f32 v42, v34, v35 op_sel:[0,0,1]
	v_cvt_pk_fp8_f32 v43, v38, v39 op_sel:[0,0,1]
	s_nop 1
	v_permlane32_swap_b32_e32 v40, v42
	v_permlane32_swap_b32_e32 v41, v43
	s_nop 1
	v_permlane16_swap_b32_e32 v40, v41
	v_permlane16_swap_b32_e32 v42, v43
	global_store_dwordx4 v[252:253], v[40:43], off
	v_lshl_add_u64 v[252:253], v[252:253], 0, s[100:101]
	v_med3_f32 v24, v92, s77, v200
	v_med3_f32 v25, v93, s77, v200
	v_med3_f32 v26, v94, s77, v200
	v_med3_f32 v27, v95, s77, v200
	v_med3_f32 v28, v88, s77, v200
	v_med3_f32 v29, v89, s77, v200
	v_med3_f32 v30, v90, s77, v200
	v_med3_f32 v31, v91, s77, v200
	v_med3_f32 v32, v60, s77, v200
	v_med3_f32 v33, v61, s77, v200
	v_med3_f32 v34, v62, s77, v200
	v_med3_f32 v35, v63, s77, v200
	v_med3_f32 v36, v56, s77, v200
	v_med3_f32 v37, v57, s77, v200
	v_med3_f32 v38, v58, s77, v200
	v_med3_f32 v39, v59, s77, v200
	v_cvt_pk_fp8_f32 v20, v24, v25
	v_cvt_pk_fp8_f32 v21, v28, v29
	v_cvt_pk_fp8_f32 v22, v32, v33
	v_cvt_pk_fp8_f32 v23, v36, v37
	v_cvt_pk_fp8_f32 v20, v26, v27 op_sel:[0,0,1]
	v_cvt_pk_fp8_f32 v21, v30, v31 op_sel:[0,0,1]
	v_cvt_pk_fp8_f32 v22, v34, v35 op_sel:[0,0,1]
	v_cvt_pk_fp8_f32 v23, v38, v39 op_sel:[0,0,1]
	s_nop 1
	v_permlane32_swap_b32_e32 v20, v22
	v_permlane32_swap_b32_e32 v21, v23
	s_nop 1
	v_permlane16_swap_b32_e32 v20, v21
	v_permlane16_swap_b32_e32 v22, v23
	global_store_dwordx4 v[252:253], v[20:23], off
	v_lshl_add_u64 v[252:253], v[252:253], 0, s[100:101]
	v_med3_f32 v24, v84, s77, v200
	v_med3_f32 v25, v85, s77, v200
	v_med3_f32 v26, v86, s77, v200
	v_med3_f32 v27, v87, s77, v200
	v_med3_f32 v28, v80, s77, v200
	v_med3_f32 v29, v81, s77, v200
	v_med3_f32 v30, v82, s77, v200
	v_med3_f32 v31, v83, s77, v200
	v_med3_f32 v32, v52, s77, v200
	v_med3_f32 v33, v53, s77, v200
	v_med3_f32 v34, v54, s77, v200
	v_med3_f32 v35, v55, s77, v200
	v_med3_f32 v36, v48, s77, v200
	v_med3_f32 v37, v49, s77, v200
	v_med3_f32 v38, v50, s77, v200
	v_med3_f32 v39, v51, s77, v200
	v_cvt_pk_fp8_f32 v40, v24, v25
	v_cvt_pk_fp8_f32 v41, v28, v29
	v_cvt_pk_fp8_f32 v42, v32, v33
	v_cvt_pk_fp8_f32 v43, v36, v37
	v_cvt_pk_fp8_f32 v40, v26, v27 op_sel:[0,0,1]
	v_cvt_pk_fp8_f32 v41, v30, v31 op_sel:[0,0,1]
	v_cvt_pk_fp8_f32 v42, v34, v35 op_sel:[0,0,1]
	v_cvt_pk_fp8_f32 v43, v38, v39 op_sel:[0,0,1]
	s_nop 1
	v_permlane32_swap_b32_e32 v40, v42
	v_permlane32_swap_b32_e32 v41, v43
	s_nop 1
	v_permlane16_swap_b32_e32 v40, v41
	v_permlane16_swap_b32_e32 v42, v43
	global_store_dwordx4 v[252:253], v[40:43], off
	s_cbranch_vccnz .LBB0_994
	s_mov_b32 s81, s79
	s_mov_b64 s[8:9], s[22:23]
	s_mov_b32 s6, s20
	s_mov_b32 s44, s82
	s_mov_b32 s10, s21
	s_mov_b32 s80, s71
	s_waitcnt vmcnt(8)
	v_mov_b64_e32 v[164:165], v[172:173]
	v_mov_b64_e32 v[166:167], v[174:175]
	v_mov_b64_e32 v[160:161], v[168:169]
	v_mov_b64_e32 v[162:163], v[170:171]
	v_mov_b64_e32 v[156:157], v[172:173]
	v_mov_b64_e32 v[158:159], v[174:175]
	v_mov_b64_e32 v[152:153], v[168:169]
	v_mov_b64_e32 v[154:155], v[170:171]
	v_mov_b64_e32 v[148:149], v[172:173]
	v_mov_b64_e32 v[150:151], v[174:175]
	v_mov_b64_e32 v[144:145], v[168:169]
	v_mov_b64_e32 v[146:147], v[170:171]
	v_mov_b64_e32 v[132:133], v[140:141]
	v_mov_b64_e32 v[134:135], v[142:143]
	v_mov_b64_e32 v[128:129], v[136:137]
	v_mov_b64_e32 v[130:131], v[138:139]
	v_mov_b64_e32 v[124:125], v[140:141]
	v_mov_b64_e32 v[126:127], v[142:143]
	v_mov_b64_e32 v[120:121], v[136:137]
	v_mov_b64_e32 v[122:123], v[138:139]
	v_mov_b64_e32 v[116:117], v[140:141]
	v_mov_b64_e32 v[118:119], v[142:143]
	v_mov_b64_e32 v[112:113], v[136:137]
	v_mov_b64_e32 v[114:115], v[138:139]
	v_mov_b64_e32 v[108:109], v[172:173]
	v_mov_b64_e32 v[110:111], v[174:175]
	v_mov_b64_e32 v[104:105], v[168:169]
	v_mov_b64_e32 v[106:107], v[170:171]
	v_mov_b64_e32 v[100:101], v[172:173]
	v_mov_b64_e32 v[102:103], v[174:175]
	v_mov_b64_e32 v[96:97], v[168:169]
	v_mov_b64_e32 v[98:99], v[170:171]
	v_mov_b64_e32 v[92:93], v[172:173]
	v_mov_b64_e32 v[94:95], v[174:175]
	v_mov_b64_e32 v[88:89], v[168:169]
	v_mov_b64_e32 v[90:91], v[170:171]
	v_mov_b64_e32 v[84:85], v[172:173]
	v_mov_b64_e32 v[86:87], v[174:175]
	v_mov_b64_e32 v[80:81], v[168:169]
	v_mov_b64_e32 v[82:83], v[170:171]
	v_mov_b64_e32 v[76:77], v[140:141]
	v_mov_b64_e32 v[78:79], v[142:143]
	v_mov_b64_e32 v[72:73], v[136:137]
	v_mov_b64_e32 v[74:75], v[138:139]
	v_mov_b64_e32 v[68:69], v[140:141]
	v_mov_b64_e32 v[70:71], v[142:143]
	v_mov_b64_e32 v[64:65], v[136:137]
	v_mov_b64_e32 v[66:67], v[138:139]
	v_mov_b64_e32 v[60:61], v[140:141]
	v_mov_b64_e32 v[62:63], v[142:143]
	v_mov_b64_e32 v[56:57], v[136:137]
	v_mov_b64_e32 v[58:59], v[138:139]
	v_mov_b64_e32 v[52:53], v[140:141]
	v_mov_b64_e32 v[54:55], v[142:143]
	v_mov_b64_e32 v[48:49], v[136:137]
	v_mov_b64_e32 v[50:51], v[138:139]
	s_branch .LBB0_994
